# MoE unit lists cut at row-tile boundaries per XCD (ceil(ntiles/8) row tiles per XCD in P7 and P8); the P7->P8 grid barrier becomes an XCD-local barrier (full barrier if the placement flag is raised)
# speedup vs baseline: 1.0175x; 1.0059x over previous
.LBB0_1180:
	v_readlane_b32 s0, v255, 3
	v_readlane_b32 s1, v255, 4
	s_add_u32 s10, s90, 0xc900000
	s_addc_u32 s11, s91, 0
	v_cndmask_b32_e64 v2, 0, 1, s[0:1]
	s_andn2_b64 vcc, exec, s[12:13]
	v_cmp_ne_u32_e64 s[26:27], 1, v2
	s_cbranch_vccnz .LBB0_1232
	s_add_i32 s0, 0, 0x20510
	s_movk_i32 s14, 0x200
	v_mov_b32_e32 v2, s0
	ds_read_b32 v2, v2
	s_ashr_i32 s35, s89, 3
	s_and_b32 s6, s89, 7
	v_readfirstlane_b32 s7, v0
	s_mov_b64 s[0:1], -1
	s_waitcnt lgkmcnt(0)
	v_readfirstlane_b32 s34, v2
	s_add_i32 s32, s34, 7
	s_ashr_i32 s32, s32, 3
	s_lshl_b32 s32, s32, 3
	s_and_b64 vcc, exec, s[26:27]
	v_readlane_b32 s4, v255, 7
	s_cbranch_vccnz .LBB0_1184
	s_cmp_lt_i32 s35, s32
	s_cbranch_scc0 .LBB0_1188
	s_mul_i32 s0, s32, s6
	s_add_i32 s4, s0, s35
	s_mov_b64 s[0:1], -1

.LBB0_1195:
	s_add_u32 s26, s90, 0x7800080
	s_mov_b64 s[38:39], 0x80
	s_addc_u32 s27, s91, 0
	s_add_i32 m0, s84, 0x18000
	v_lshl_add_u64 v[8:9], v[8:9], 0, s[38:39]
	s_waitcnt vmcnt(2)
	s_barrier
	global_load_lds_dwordx4 v[8:9], off
	v_lshl_add_u64 v[6:7], v[6:7], 0, s[38:39]
	s_add_i32 m0, s84, 0x1a000
	s_add_i32 s90, s84, 0x8000
	global_load_lds_dwordx4 v[6:7], off
	v_lshl_add_u64 v[6:7], s[26:27], 0, v[156:157]
	s_mov_b32 m0, s90
	s_add_i32 s91, s84, 0xa000
	global_load_lds_dwordx4 v[6:7], off
	v_lshl_add_u64 v[6:7], s[26:27], 0, v[158:159]
	s_mov_b32 m0, s91
	v_lshl_add_u64 v[4:5], v[4:5], 0, s[38:39]
	global_load_lds_dwordx4 v[6:7], off
	s_add_i32 m0, s84, 0x1c000
	v_lshl_add_u64 v[2:3], v[2:3], 0, s[38:39]
	global_load_lds_dwordx4 v[4:5], off
	s_add_i32 m0, s84, 0x1e000
	v_and_b32_e32 v12, 48, v0
	global_load_lds_dwordx4 v[2:3], off
	v_lshlrev_b32_e32 v13, 6, v0
	s_movk_i32 s4, 0x3c0
	v_and_or_b32 v12, v13, s4, v12
	s_add_i32 s4, 0, 0x21800
	v_lshl_add_u32 v180, v10, 2, s4
	v_readlane_b32 s4, v255, 2
	s_ashr_i32 s88, s4, 3
	s_lshr_b32 s4, s15, 26
	s_lshl_b32 s0, s0, 5
	s_add_i32 s4, s14, s4
	s_and_b32 s92, s0, 0x60
	v_and_b32_e32 v11, 32, v11
	s_ashr_i32 s15, s4, 6
	s_lshl_b32 s89, s1, 6
	s_lshl_b32 s1, s1, 13
	s_lshl_b32 s0, s92, 7
	v_bitop3_b32 v10, v12, s1, v11 bitop3:0xde
	v_bitop3_b32 v157, s0, v12, v11 bitop3:0xf6
	s_cmp_gt_i32 s14, 63
	v_readlane_b32 s0, v255, 5
	s_cselect_b64 s[42:43], -1, 0
	s_cmpk_lt_u32 s7, 0x100
	v_readlane_b32 s1, v255, 6
	s_cselect_b64 s[46:47], -1, 0
	v_mov_b32_e32 v3, 0
	v_cndmask_b32_e64 v6, 0, 1, s[0:1]
	s_add_i32 s0, 0, 0x20494
	v_writelane_b32 v255, s0, 58
	s_add_i32 s0, 0, 0x2049c
	v_writelane_b32 v255, s0, 57
	s_add_i32 s0, 0, 0x204a4
	v_writelane_b32 v255, s0, 14
	s_add_i32 s0, 0, 0x204ac
	v_writelane_b32 v255, s0, 48
	s_add_i32 s0, 0, 0x204b4
	v_writelane_b32 v255, s0, 50
	s_add_i32 s0, 0, 0x204bc
	v_writelane_b32 v255, s0, 60
	s_add_i32 s0, 0, 0x204c4
	v_writelane_b32 v255, s0, 39
	s_add_i32 s0, 0, 0x204cc
	v_writelane_b32 v255, s0, 19
	s_add_i32 s0, 0, 0x204d4
	v_writelane_b32 v255, s0, 41
	s_add_i32 s0, 0, 0x204dc
	v_writelane_b32 v255, s0, 31
	s_add_i32 s0, 0, 0x204e4
	v_writelane_b32 v255, s0, 43
	s_add_i32 s0, 0, 0x204ec
	v_writelane_b32 v255, s0, 44
	s_add_i32 s0, 0, 0x204f4
	v_writelane_b32 v255, s0, 52
	s_add_i32 s0, 0, 0x204fc
	s_waitcnt vmcnt(6)
	v_mov_b32_e32 v4, v3
	v_mov_b32_e32 v5, v3
	v_writelane_b32 v255, s0, 54
	s_add_i32 s0, 0, 0x20504
	v_mov_b32_e32 v2, v3
	v_cmp_ne_u32_e64 s[4:5], 1, v6
	v_writelane_b32 v255, s0, 37
	s_add_i32 s0, 0, 0x2050c
	v_add_u32_e32 v159, 0, v10
	v_mov_b64_e32 v[8:9], v[4:5]
	v_mov_b64_e32 v[12:13], v[4:5]
	v_mov_b64_e32 v[16:17], v[4:5]
	v_mov_b64_e32 v[20:21], v[4:5]
	v_mov_b64_e32 v[24:25], v[4:5]
	v_mov_b64_e32 v[28:29], v[4:5]
	v_mov_b64_e32 v[32:33], v[4:5]
	v_mov_b64_e32 v[36:37], v[4:5]
	v_mov_b64_e32 v[40:41], v[4:5]
	v_mov_b64_e32 v[44:45], v[4:5]
	v_mov_b64_e32 v[48:49], v[4:5]
	v_mov_b64_e32 v[52:53], v[4:5]
	v_mov_b64_e32 v[56:57], v[4:5]
	v_mov_b64_e32 v[60:61], v[4:5]
	v_mov_b64_e32 v[64:65], v[4:5]
	v_mov_b64_e32 v[68:69], v[4:5]
	v_mov_b64_e32 v[72:73], v[4:5]
	v_mov_b64_e32 v[76:77], v[4:5]
	v_mov_b64_e32 v[80:81], v[4:5]
	v_mov_b64_e32 v[84:85], v[4:5]
	v_mov_b64_e32 v[88:89], v[4:5]
	v_mov_b64_e32 v[92:93], v[4:5]
	v_mov_b64_e32 v[96:97], v[4:5]
	v_mov_b64_e32 v[100:101], v[4:5]
	v_mov_b64_e32 v[104:105], v[4:5]
	v_mov_b64_e32 v[108:109], v[4:5]
	v_mov_b64_e32 v[112:113], v[4:5]
	v_mov_b64_e32 v[116:117], v[4:5]
	v_mov_b64_e32 v[120:121], v[4:5]
	v_mov_b64_e32 v[124:125], v[4:5]
	v_mov_b64_e32 v[128:129], v[4:5]
	v_mov_b64_e32 v[132:133], v[4:5]
	v_lshlrev_b32_e32 v179, 2, v1
	s_mul_i32 s25, s32, s6
	s_add_i32 s94, s15, -4
	s_add_i32 s95, s15, -2
	v_writelane_b32 v255, s0, 56
	s_add_i32 s97, 0, 0x10000
	s_add_i32 s8, 0, 0x14000
	v_mov_b32_e32 v181, 0x7a7a7a7a
	v_mov_b32_e32 v182, 0x7f7f7f7f
	s_mov_b32 s50, 0xc01d265f
	s_mov_b32 s9, 0xc0c00000
	v_mov_b32_e32 v183, 0x41000000
	v_mov_b64_e32 v[6:7], v[2:3]
	v_mov_b64_e32 v[10:11], v[2:3]
	v_mov_b64_e32 v[14:15], v[2:3]
	v_mov_b64_e32 v[18:19], v[2:3]
	v_mov_b64_e32 v[22:23], v[2:3]
	v_mov_b64_e32 v[26:27], v[2:3]
	v_mov_b64_e32 v[30:31], v[2:3]
	v_mov_b64_e32 v[34:35], v[2:3]
	v_mov_b64_e32 v[38:39], v[2:3]
	v_mov_b64_e32 v[42:43], v[2:3]
	v_mov_b64_e32 v[46:47], v[2:3]
	v_mov_b64_e32 v[50:51], v[2:3]
	v_mov_b64_e32 v[54:55], v[2:3]
	v_mov_b64_e32 v[58:59], v[2:3]
	v_mov_b64_e32 v[62:63], v[2:3]
	v_mov_b64_e32 v[66:67], v[2:3]
	v_mov_b64_e32 v[70:71], v[2:3]
	v_mov_b64_e32 v[74:75], v[2:3]
	v_mov_b64_e32 v[78:79], v[2:3]
	v_mov_b64_e32 v[82:83], v[2:3]
	v_mov_b64_e32 v[86:87], v[2:3]
	v_mov_b64_e32 v[90:91], v[2:3]
	v_mov_b64_e32 v[94:95], v[2:3]
	v_mov_b64_e32 v[98:99], v[2:3]
	v_mov_b64_e32 v[102:103], v[2:3]
	v_mov_b64_e32 v[106:107], v[2:3]
	v_mov_b64_e32 v[110:111], v[2:3]
	v_mov_b64_e32 v[114:115], v[2:3]
	v_mov_b64_e32 v[118:119], v[2:3]
	v_mov_b64_e32 v[122:123], v[2:3]
	v_mov_b64_e32 v[126:127], v[2:3]
	v_mov_b64_e32 v[130:131], v[2:3]
	v_mov_b32_e32 v184, v156
	v_mov_b32_e32 v185, v158
	v_mov_b32_e32 v4, v177
	v_mov_b32_e32 v162, v178
	s_mov_b32 s96, 0
	s_barrier
	s_branch .LBB0_1198

.LBB0_1200:
	s_andn2_b64 vcc, exec, s[6:7]
	s_cbranch_vccnz .LBB0_1203
	s_mul_i32 s6, s93, s88
	s_add_i32 s6, s6, s35
	s_cmp_lt_i32 s6, s32
	s_cbranch_scc0 .LBB0_1203
	s_add_i32 s22, s6, s25
	s_mov_b64 s[0:1], -1

.LBB0_1232:
	s_cmp_gt_i32 s81, 8
	s_cselect_b64 s[0:1], -1, 0
	s_and_b64 s[2:3], s[12:13], s[0:1]
	s_andn2_b64 vcc, exec, s[2:3]
	s_cbranch_vccnz .LBB0_1284
	s_waitcnt vmcnt(0)
	s_waitcnt vmcnt(0) lgkmcnt(0)
	s_barrier
	s_mov_b64 s[4:5], exec
	v_readlane_b32 s2, v255, 12
	v_readlane_b32 s3, v255, 13
	s_and_b64 s[2:3], s[4:5], s[2:3]
	s_mov_b64 exec, s[2:3]
	s_cbranch_execz .LBB0_1283
	v_readlane_b32 s8, v255, 11
	v_readlane_b32 s12, v255, 9
	v_readlane_b32 s13, v255, 10
	v_mov_b32_e32 v4, 0x20160
	ds_read_b32 v4, v4
	s_lshl_b32 s8, s8, 8
	s_add_u32 s8, s12, s8
	s_addc_u32 s9, s13, 0
	v_mov_b32_e32 v5, 0x2000
	v_mov_b32_e32 v6, 1
	v_mov_b32_e32 v2, 0x3000
	s_mov_b32 s2, 0
	global_atomic_add v5, v6, s[8:9] offset:1024
	buffer_inv sc1
	global_load_dword v2, v2, s[12:13] offset:896 sc1
	s_waitcnt lgkmcnt(0)
	v_mul_u32_u24_e32 v4, 3, v4
.Lxl_spin_2:
	global_load_dword v6, v5, s[8:9] offset:1024 sc1
	s_waitcnt vmcnt(0)
	v_cmp_ne_u32_e32 vcc, 0, v2
	s_cbranch_vccnz .Lxl_full_2
	v_cmp_ge_u32_e32 vcc, v6, v4
	s_cbranch_vccnz .LBB0_1283
	s_sleep 1
	s_add_u32 s2, s2, 1
	s_cmp_lt_u32 s2, 0x40000
	s_cbranch_scc1 .Lxl_spin_2
	s_branch .LBB0_1283
.Lxl_full_2:
	s_add_i32 s2, 0, 0x20160
	v_mov_b32_e32 v2, s2
	s_waitcnt vmcnt(0) expcnt(0) lgkmcnt(0)
	ds_read_b32 v4, v2
	s_add_i32 s2, 0, 0x20164
	v_mov_b32_e32 v2, s2
	ds_read_b32 v2, v2
	s_waitcnt lgkmcnt(1)
	v_cmp_ne_u32_e32 vcc, 0, v4
	s_cbranch_vccnz .LBB0_1249
	v_readlane_b32 s2, v255, 0
	v_readlane_b32 s3, v255, 1
	s_load_dwordx2 s[8:9], s[2:3], 0x4
	v_readlane_b32 s14, v255, 9
	v_readlane_b32 s15, v255, 10
	s_add_u32 s2, s14, 0x1000
	s_addc_u32 s3, s15, 0
	s_add_u32 s6, s14, 0x1100
	s_addc_u32 s7, s15, 0
	v_readlane_b32 s12, v255, 2
	s_waitcnt lgkmcnt(0)
	s_mul_i32 s8, s8, s12
	s_add_u32 s12, s14, 0x1200
	s_addc_u32 s13, s15, 0
	s_add_u32 s14, s14, 0x1300
	s_mul_i32 s8, s8, s9
	s_addc_u32 s15, s15, 0
	s_mov_b32 s9, 1
	v_mov_b32_e32 v18, 0
	s_branch .LBB0_1237

.LBB0_1284:
	s_cmp_lt_i32 s80, 9
	s_cselect_b64 s[2:3], -1, 0
	s_add_u32 s12, s90, 0x11000000
	s_addc_u32 s13, s91, 0
	s_and_b64 s[14:15], s[2:3], s[0:1]
	s_andn2_b64 vcc, exec, s[14:15]
	s_cbranch_vccnz .LBB0_1341
	s_add_i32 s1, 0, 0x20510
	s_movk_i32 s0, 0x200
	v_mov_b32_e32 v2, s1
	ds_read_b32 v2, v2
	s_ashr_i32 s33, s89, 3
	s_and_b32 s6, s89, 7
	v_readfirstlane_b32 s7, v0
	s_and_b64 vcc, exec, s[26:27]
	s_waitcnt lgkmcnt(0)
	v_readfirstlane_b32 s1, v2
	s_lshl_b32 s34, s1, 2
	s_mov_b64 s[2:3], -1
	s_cbranch_vccnz .LBB0_1288
	s_add_i32 s1, s34, 31
	s_ashr_i32 s1, s1, 5
	s_lshl_b32 s1, s1, 2
	s_cmp_lt_i32 s33, s1
	s_cbranch_scc0 .LBB0_1292
	s_mul_i32 s1, s1, s6
	s_add_i32 s1, s1, s33
	v_writelane_b32 v255, s1, 7

.LBB0_1299:
	s_lshr_b32 s1, s1, 26
	v_and_b32_e32 v20, 15, v0
	v_and_b32_e32 v21, 48, v0
	v_lshlrev_b32_e32 v22, 6, v0
	v_lshlrev_b32_e32 v0, 2, v0
	s_add_i32 s1, s0, s1
	v_lshrrev_b32_e32 v19, 4, v1
	v_and_b32_e32 v0, 32, v0
	v_bfe_u32 v168, v1, 4, 1
	s_ashr_i32 s73, s1, 6
	v_lshl_or_b32 v1, v20, 6, v21
	s_lshl_b32 s1, s2, 13
	v_lshl_or_b32 v169, s2, 6, v20
	v_bitop3_b32 v20, v1, s1, v0 bitop3:0xde
	s_lshl_b32 s1, s3, 5
	s_movk_i32 s4, 0x3c0
	s_and_b32 s1, s1, 0x60
	v_and_or_b32 v22, v22, s4, v21
	s_lshl_b32 s2, s1, 7
	s_mov_b64 s[26:27], 0x80
	v_bitop3_b32 v170, s2, v22, v0 bitop3:0xf6
	s_add_i32 m0, s68, 0x18000
	v_lshl_add_u64 v[0:1], v[12:13], 0, s[26:27]
	s_waitcnt vmcnt(2)
	s_barrier
	global_load_lds_dwordx4 v[0:1], off
	v_lshl_add_u64 v[0:1], v[8:9], 0, s[26:27]
	s_add_i32 m0, s68, 0x1a000
	s_add_i32 s75, s68, 0x8000
	global_load_lds_dwordx4 v[0:1], off
	v_lshl_add_u64 v[0:1], v[10:11], 0, s[26:27]
	s_mov_b32 m0, s75
	s_add_i32 s76, s68, 0xa000
	global_load_lds_dwordx4 v[0:1], off
	v_lshl_add_u64 v[0:1], v[14:15], 0, s[26:27]
	s_mov_b32 m0, s76
	v_readlane_b32 s4, v255, 2
	global_load_lds_dwordx4 v[0:1], off
	s_add_i32 m0, s68, 0x1c000
	v_lshl_add_u64 v[0:1], v[6:7], 0, s[26:27]
	global_load_lds_dwordx4 v[0:1], off
	v_lshl_add_u64 v[0:1], v[4:5], 0, s[26:27]
	s_add_i32 m0, s68, 0x1e000
	s_ashr_i32 s72, s4, 3
	global_load_lds_dwordx4 v[0:1], off
	s_cmp_gt_i32 s0, 63
	s_cselect_b64 s[38:39], -1, 0
	s_add_i32 s77, s73, -2
	s_cmpk_lt_u32 s7, 0x100
	s_cselect_b64 s[42:43], -1, 0
	v_lshl_or_b32 v171, v19, 3, s1
	s_add_i32 s1, s34, 31
	s_ashr_i32 s78, s1, 5
	s_lshl_b32 s78, s78, 2
	v_add_u32_e32 v0, v17, v3
	s_mul_i32 s1, s78, s6
	v_mad_u64_u32 v[0:1], s[2:3], s0, v0, v[2:3]
	v_writelane_b32 v255, s1, 16
	s_add_i32 s1, 0, 0x21000
	v_add_lshl_u32 v8, v0, v16, 1
	v_add_u32_e32 v0, v18, v3
	v_lshl_add_u32 v173, v171, 2, s1
	v_mad_u64_u32 v[0:1], s[0:1], s0, v0, v[2:3]
	v_readlane_b32 s0, v255, 5
	v_mov_b32_e32 v9, 0
	v_readlane_b32 s1, v255, 6
	v_lshl_add_u64 v[162:163], s[20:21], 0, v[8:9]
	v_add_lshl_u32 v8, v0, v16, 1
	v_cndmask_b32_e64 v0, 0, 1, s[0:1]
	s_add_i32 s0, 0, 0x20494
	v_writelane_b32 v255, s0, 58
	s_add_i32 s0, 0, 0x2049c
	s_waitcnt vmcnt(6)
	v_mov_b32_e32 v10, v9
	v_mov_b32_e32 v11, v9
	v_writelane_b32 v255, s0, 57
	s_add_i32 s0, 0, 0x204a4
	v_lshl_add_u64 v[164:165], s[20:21], 0, v[8:9]
	v_mov_b32_e32 v8, v9
	v_writelane_b32 v255, s0, 14
	s_add_i32 s0, 0, 0x204ac
	v_add_u32_e32 v174, 0, v20
	v_mov_b64_e32 v[14:15], v[10:11]
	v_mov_b64_e32 v[18:19], v[10:11]
	v_mov_b64_e32 v[22:23], v[10:11]
	v_mov_b64_e32 v[26:27], v[10:11]
	v_mov_b64_e32 v[30:31], v[10:11]
	v_mov_b64_e32 v[34:35], v[10:11]
	v_mov_b64_e32 v[38:39], v[10:11]
	v_mov_b64_e32 v[42:43], v[10:11]
	v_mov_b64_e32 v[46:47], v[10:11]
	v_mov_b64_e32 v[50:51], v[10:11]
	v_mov_b64_e32 v[54:55], v[10:11]
	v_mov_b64_e32 v[58:59], v[10:11]
	v_mov_b64_e32 v[62:63], v[10:11]
	v_mov_b64_e32 v[66:67], v[10:11]
	v_mov_b64_e32 v[70:71], v[10:11]
	v_mov_b64_e32 v[74:75], v[10:11]
	v_mov_b64_e32 v[78:79], v[10:11]
	v_mov_b64_e32 v[82:83], v[10:11]
	v_mov_b64_e32 v[86:87], v[10:11]
	v_mov_b64_e32 v[90:91], v[10:11]
	v_mov_b64_e32 v[94:95], v[10:11]
	v_mov_b64_e32 v[98:99], v[10:11]
	v_mov_b64_e32 v[102:103], v[10:11]
	v_mov_b64_e32 v[106:107], v[10:11]
	v_mov_b64_e32 v[110:111], v[10:11]
	v_mov_b64_e32 v[114:115], v[10:11]
	v_mov_b64_e32 v[118:119], v[10:11]
	v_mov_b64_e32 v[122:123], v[10:11]
	v_mov_b64_e32 v[126:127], v[10:11]
	v_mov_b64_e32 v[130:131], v[10:11]
	v_mov_b64_e32 v[134:135], v[10:11]
	v_mov_b64_e32 v[138:139], v[10:11]
	v_add_u32_e32 v172, 0x80, v169
	v_cmp_ne_u32_e64 s[6:7], 1, v0
	v_writelane_b32 v255, s0, 48
	s_add_i32 s84, 0, 0x204b4
	s_add_i32 s85, 0, 0x204bc
	s_add_i32 s86, 0, 0x204c4
	s_add_i32 s87, 0, 0x204cc
	s_add_i32 s88, 0, 0x204d4
	s_add_i32 s89, 0, 0x204dc
	s_add_i32 s90, 0, 0x204e4
	s_add_i32 s91, 0, 0x204ec
	s_add_i32 s92, 0, 0x204f4
	s_add_i32 s93, 0, 0x204fc
	s_add_i32 s94, 0, 0x20504
	s_add_i32 s95, 0, 0x2050c
	s_add_i32 s96, 0, 0x10000
	s_add_i32 s97, 0, 0x14000
	v_mov_b32_e32 v175, 0x7a7a7a7a
	v_mov_b32_e32 v176, 0x7f7f7f7f
	v_mov_b64_e32 v[12:13], v[8:9]
	v_mov_b64_e32 v[16:17], v[8:9]
	v_mov_b64_e32 v[20:21], v[8:9]
	v_mov_b64_e32 v[24:25], v[8:9]
	v_mov_b64_e32 v[28:29], v[8:9]
	v_mov_b64_e32 v[32:33], v[8:9]
	v_mov_b64_e32 v[36:37], v[8:9]
	v_mov_b64_e32 v[40:41], v[8:9]
	v_mov_b64_e32 v[44:45], v[8:9]
	v_mov_b64_e32 v[48:49], v[8:9]
	v_mov_b64_e32 v[52:53], v[8:9]
	v_mov_b64_e32 v[56:57], v[8:9]
	v_mov_b64_e32 v[60:61], v[8:9]
	v_mov_b64_e32 v[64:65], v[8:9]
	v_mov_b64_e32 v[68:69], v[8:9]
	v_mov_b64_e32 v[72:73], v[8:9]
	v_mov_b64_e32 v[76:77], v[8:9]
	v_mov_b64_e32 v[80:81], v[8:9]
	v_mov_b64_e32 v[84:85], v[8:9]
	v_mov_b64_e32 v[88:89], v[8:9]
	v_mov_b64_e32 v[92:93], v[8:9]
	v_mov_b64_e32 v[96:97], v[8:9]
	v_mov_b64_e32 v[100:101], v[8:9]
	v_mov_b64_e32 v[104:105], v[8:9]
	v_mov_b64_e32 v[108:109], v[8:9]
	v_mov_b64_e32 v[112:113], v[8:9]
	v_mov_b64_e32 v[116:117], v[8:9]
	v_mov_b64_e32 v[120:121], v[8:9]
	v_mov_b64_e32 v[124:125], v[8:9]
	v_mov_b64_e32 v[128:129], v[8:9]
	v_mov_b64_e32 v[132:133], v[8:9]
	v_mov_b64_e32 v[136:137], v[8:9]
	s_barrier
	s_branch .LBB0_1302
